# FoX epilogue: gate prefetch chain extended to the last output row (row 15); placement kept
# speedup vs baseline: 1.0022x; 1.0022x over previous
; __device__ __forceinline__ unsigned cvt_pk_bf16(float lo, float hi) { unsigned r; asm volatile("v_cvt_pk_bf16_f32 %0, %1, %2" : "=v"(r) : "v"(lo), "v"(hi)); return r; }
; __device__ __forceinline__ float bf_lo(unsigned w) { return __uint_as_float(w << 16); }
; __device__ __forceinline__ float bf_hi(unsigned w) { return __uint_as_float(w & 0xffff0000u); }
; __device__ __forceinline__ int crow(int r, int hi) { return (r & 3) + 8 * (r >> 2) + 4 * hi; }
; template <int MODE> ...
;     ...
;     for (int r = 0; r < 16; ++r) { const int orow = qlo + crow(r, hi); const float rl = __builtin_amdgcn_rcpf(li_l[crow(r, hi)]);
; #pragma unroll
;         for (int d0 = 0; d0 < 4; ++d0) { float v = o[d0][r] * rl; float vn = __shfl_xor(v, 1);
;             if ((r32 & 1) == 0) { const int col = d0 * 32 + r32;
;                 if (MODE == 1) { const unsigned g = *(const unsigned*)(gate + (size_t)orow * 1024 + hoff + col); v *= bf_lo(g); vn *= bf_hi(g); }
;                 *(unsigned*)(Ob + (size_t)orow * DM + ocol0 + col) = cvt_pk_bf16(v, vn); } } }
.LBB0_1524:
	s_or_b64 exec, exec, s[0:1]
	ds_read_b32 v5, v160 offset:104
	v_add_u32_e32 v6, 26, v4
	v_ashrrev_i32_e32 v7, 31, v6
	v_lshlrev_b64 v[8:9], 11, v[6:7]
	v_lshlrev_b64 v[6:7], 12, v[6:7]
	s_waitcnt lgkmcnt(0)
	v_rcp_f32_e32 v5, v5
	v_lshl_add_u64 v[8:9], s[6:7], 0, v[8:9]
	v_lshl_add_u64 v[6:7], s[8:9], 0, v[6:7]
	v_add_u32_e32 v252, 27, v4
	v_ashrrev_i32_e32 v253, 31, v252
	v_lshlrev_b64 v[252:253], 11, v[252:253]
	v_lshl_add_u64 v[252:253], s[6:7], 0, v[252:253]
	v_lshl_add_u64 v[252:253], v[252:253], 0, v[2:3]
	global_load_dword v244, v[252:253], off
	global_load_dword v245, v[252:253], off offset:64
	global_load_dword v246, v[252:253], off offset:128
	global_load_dword v247, v[252:253], off offset:192
	v_mul_f32_e32 v11, v80, v5
	s_nop 1
	v_mov_b32_dpp v12, v11 quad_perm:[1,0,3,2] row_mask:0xf bank_mask:0xf
	s_and_saveexec_b64 s[0:1], s[2:3]
	s_cbranch_execz .LBB0_1526
	v_lshl_add_u64 v[14:15], v[8:9], 0, v[2:3]
	s_waitcnt vmcnt(4)
	v_mov_b32_e32 v13, v248
	v_lshlrev_b32_e32 v14, 16, v13
	v_and_b32_e32 v13, 0xffff0000, v13
	v_mul_f32_e32 v11, v11, v14
	s_waitcnt lgkmcnt(0)
	v_mul_f32_e32 v12, v12, v13
	v_cvt_pk_bf16_f32 v11, v11, v12
	v_lshl_add_u64 v[12:13], v[6:7], 0, v[2:3]
	global_store_dword v[12:13], v11, off

; __device__ __forceinline__ unsigned cvt_pk_bf16(float lo, float hi) { unsigned r; asm volatile("v_cvt_pk_bf16_f32 %0, %1, %2" : "=v"(r) : "v"(lo), "v"(hi)); return r; }
; __device__ __forceinline__ float bf_lo(unsigned w) { return __uint_as_float(w << 16); }
; __device__ __forceinline__ float bf_hi(unsigned w) { return __uint_as_float(w & 0xffff0000u); }
; __device__ __forceinline__ int crow(int r, int hi) { return (r & 3) + 8 * (r >> 2) + 4 * hi; }
; template <int MODE> ...
;     ...
;     for (int r = 0; r < 16; ++r) { const int orow = qlo + crow(r, hi); const float rl = __builtin_amdgcn_rcpf(li_l[crow(r, hi)]);
; #pragma unroll
;         for (int d0 = 0; d0 < 4; ++d0) { float v = o[d0][r] * rl; float vn = __shfl_xor(v, 1);
;             if ((r32 & 1) == 0) { const int col = d0 * 32 + r32;
;                 if (MODE == 1) { const unsigned g = *(const unsigned*)(gate + (size_t)orow * 1024 + hoff + col); v *= bf_lo(g); vn *= bf_hi(g); }
;                 *(unsigned*)(Ob + (size_t)orow * DM + ocol0 + col) = cvt_pk_bf16(v, vn); } } }
.LBB0_1532:
	s_or_b64 exec, exec, s[0:1]
	ds_read_b32 v5, v160 offset:108
	v_add_u32_e32 v4, 27, v4
	s_waitcnt lgkmcnt(0)
	v_rcp_f32_e32 v8, v5
	v_ashrrev_i32_e32 v5, 31, v4
	v_lshlrev_b64 v[6:7], 11, v[4:5]
	v_lshlrev_b64 v[4:5], 12, v[4:5]
	v_mul_f32_e32 v9, v81, v8
	s_nop 1
	v_mov_b32_dpp v11, v9 quad_perm:[1,0,3,2] row_mask:0xf bank_mask:0xf
	v_lshl_add_u64 v[6:7], s[6:7], 0, v[6:7]
	v_lshl_add_u64 v[4:5], s[8:9], 0, v[4:5]
	s_and_saveexec_b64 s[0:1], s[2:3]
	s_cbranch_execz .LBB0_1534
	v_lshl_add_u64 v[12:13], v[6:7], 0, v[2:3]
	s_waitcnt vmcnt(0)
	v_mov_b32_e32 v12, v244
	v_lshlrev_b32_e32 v13, 16, v12
	v_and_b32_e32 v12, 0xffff0000, v12
	v_mul_f32_e32 v9, v9, v13
	s_waitcnt lgkmcnt(0)
	v_mul_f32_e32 v11, v11, v12
	v_lshl_add_u64 v[12:13], v[4:5], 0, v[2:3]
	v_cvt_pk_bf16_f32 v9, v9, v11
	global_store_dword v[12:13], v9, off
.LBB0_1534:
	s_or_b64 exec, exec, s[0:1]
	v_mul_f32_e32 v9, v65, v8
	s_waitcnt lgkmcnt(0)
	s_nop 1
	v_mov_b32_dpp v11, v9 quad_perm:[1,0,3,2] row_mask:0xf bank_mask:0xf
	s_and_saveexec_b64 s[0:1], s[2:3]
	s_cbranch_execz .LBB0_1536
	v_lshl_add_u64 v[12:13], v[6:7], 0, v[2:3]
	v_mov_b32_e32 v12, v245
	v_lshlrev_b32_e32 v13, 16, v12
	v_and_b32_e32 v12, 0xffff0000, v12
	v_mul_f32_e32 v9, v9, v13
	s_waitcnt lgkmcnt(0)
	v_mul_f32_e32 v11, v11, v12
	v_lshl_add_u64 v[12:13], v[4:5], 0, v[2:3]
	v_cvt_pk_bf16_f32 v9, v9, v11
	global_store_dword v[12:13], v9, off offset:64
.LBB0_1536:
	s_or_b64 exec, exec, s[0:1]
	v_mul_f32_e32 v9, v49, v8
	s_waitcnt lgkmcnt(0)
	s_nop 1
	v_mov_b32_dpp v11, v9 quad_perm:[1,0,3,2] row_mask:0xf bank_mask:0xf
	s_and_saveexec_b64 s[0:1], s[2:3]
	s_cbranch_execz .LBB0_1538
	v_lshl_add_u64 v[12:13], v[6:7], 0, v[2:3]
	v_mov_b32_e32 v12, v246
	v_lshlrev_b32_e32 v13, 16, v12
	v_and_b32_e32 v12, 0xffff0000, v12
	v_mul_f32_e32 v9, v9, v13
	s_waitcnt lgkmcnt(0)
	v_mul_f32_e32 v11, v11, v12
	v_lshl_add_u64 v[12:13], v[4:5], 0, v[2:3]
	v_cvt_pk_bf16_f32 v9, v9, v11
	global_store_dword v[12:13], v9, off offset:128
.LBB0_1538:
	s_or_b64 exec, exec, s[0:1]
	v_mul_f32_e32 v8, v33, v8
	s_nop 1
	v_mov_b32_dpp v9, v8 quad_perm:[1,0,3,2] row_mask:0xf bank_mask:0xf
	s_and_saveexec_b64 s[0:1], s[2:3]
	s_xor_b64 s[0:1], exec, s[0:1]
	s_cbranch_execz .LBB0_1365
	v_lshl_add_u64 v[6:7], v[6:7], 0, v[2:3]
	v_lshl_add_u64 v[4:5], v[4:5], 0, v[2:3]
	v_mov_b32_e32 v6, v247
	v_lshlrev_b32_e32 v7, 16, v6
	v_and_b32_e32 v6, 0xffff0000, v6
	s_waitcnt lgkmcnt(0)
	v_mul_f32_e32 v6, v9, v6
	v_mul_f32_e32 v7, v8, v7
	v_cvt_pk_bf16_f32 v6, v7, v6
	global_store_dword v[4:5], v6, off offset:192
	s_branch .LBB0_1365

; #define PG8_STAGE(bufoff, gbase, voff) do { _Pragma("unroll") for (int _i = 0; _i < 2; ++_i) glds16_s((const void*)((const char*)(gbase) + _i * r64), (voff), ldsb + (unsigned)(bufoff) + ldsw + _i * 8192u); } while (0)
; #define PG8_WAIT_V(n) asm volatile("s_waitcnt vmcnt(" #n ")" ::: "memory")
; #define PG8_BAR __builtin_amdgcn_s_barrier()
; template <class Epi, class Sched, bool FP8 = false>
; __device__ __forceinline__ void gemm_phase(LAS unsigned char* lds, const int Kb, const int nt  , const Sched& S, const Epi& E) {
;     ...
;     PG8_STAGE(PG8_SB(0, 0), cB, voffB); PG8_STAGE(PG8_SA(0, 0), cA, voffA); PG8_STAGE(PG8_SB(0, 1), cB + hstep, voffB); PG8_STAGE(PG8_SA(0, 1), cA + hstep, voffA);
;     if (wr == 1) PG8_BAR;
;     PG8_WAIT_V(4); PG8_BAR;
;     PG8_STAGE(PG8_SB(1, 0), cB + kstep, voffB); PG8_STAGE(PG8_SA(1, 0), cA + kstep, voffA); PG8_STAGE(PG8_SB(1, 1), cB + hstep + kstep, voffB);
;     PG8_WAIT_V(6); PG8_BAR;
.LBB0_1706:
	v_readlane_b32 s4, v241, 5
	v_readlane_b32 s5, v241, 6
	s_add_u32 s4, s4, 0x56f00000
	s_addc_u32 s5, s5, 0
	s_lshl_b32 s3, s3, 5
	s_and_b32 s46, s3, 0x60
	s_lshl_b32 s45, s6, 6
	s_lshl_b32 s8, s6, 13
	s_lshl_b32 s3, s46, 7
	s_add_u32 s6, s24, 0x80
	s_addc_u32 s7, s25, 0
	s_add_i32 s47, s37, 0x18000
	s_waitcnt vmcnt(4)
	s_barrier
	s_mov_b32 s9, m0
	s_mov_b32 m0, s47
	s_nop 0
	global_load_lds_dwordx4 v1, s[6:7]
	s_mov_b32 m0, s9
	s_add_u32 s6, s24, 0x40080
	s_addc_u32 s7, s25, 0
	s_add_i32 s48, s37, 0x1a000
	s_mov_b32 s9, m0
	s_mov_b32 m0, s48
	s_nop 0
	global_load_lds_dwordx4 v1, s[6:7]
	s_mov_b32 m0, s9
	s_add_u32 s6, s22, 0x80
	s_addc_u32 s7, s23, 0
	s_add_i32 s49, s37, 0x8000
	s_mov_b32 s9, m0
	s_mov_b32 m0, s49
	s_nop 0
	global_load_lds_dwordx4 v1, s[6:7]
	s_mov_b32 m0, s9
	s_add_u32 s6, s22, 0x40080
	s_addc_u32 s7, s23, 0
	s_add_i32 s50, s37, 0xa000
	s_mov_b32 s9, m0
	s_mov_b32 m0, s50
	s_nop 0
	global_load_lds_dwordx4 v1, s[6:7]
	s_mov_b32 m0, s9
	s_add_u32 s6, s24, 0x80080
	s_addc_u32 s7, s25, 0
	s_add_i32 s51, s37, 0x1c000
	v_lshlrev_b32_e32 v3, 6, v0
	v_lshlrev_b32_e32 v4, 2, v0
	s_mov_b32 s9, m0
	s_mov_b32 m0, s51
	s_nop 0
	global_load_lds_dwordx4 v1, s[6:7]
	s_mov_b32 m0, s9
	s_add_u32 s6, s24, 0xc0080
	v_and_b32_e32 v2, 48, v0
	v_and_b32_e32 v3, 0x3c0, v3
	v_and_b32_e32 v4, 32, v4
	s_addc_u32 s7, s25, 0
	s_add_i32 s52, s37, 0x1e000
	s_mov_b32 s9, m0
	s_mov_b32 m0, s52
	s_nop 0
	global_load_lds_dwordx4 v1, s[6:7]
	s_mov_b32 m0, s9
	v_bitop3_b32 v2, v3, v4, v2 bitop3:0x36
	s_waitcnt vmcnt(6)
	s_add_i32 s3, s3, 0
	s_add_i32 s53, s37, 0xc000
	s_add_i32 s54, s37, 0xe000
	v_add_u32_e32 v3, s3, v2
	v_add_u32_e32 v2, 0, v2
	s_cmp_lg_u64 s[76:77], 0
	s_waitcnt vmcnt(5)
	v_add_u32_e32 v138, 0x10000, v3
	v_add_u32_e32 v139, 0x10400, v3
	v_add_u32_e32 v140, 0x10800, v3
	v_add_u32_e32 v141, 0x10c00, v3
	s_waitcnt vmcnt(4)
	v_add_u32_e32 v142, 0x14000, v3
	v_add_u32_e32 v143, 0x14400, v3
	v_add_u32_e32 v144, 0x14800, v3
	v_add_u32_e32 v145, 0x14c00, v3
	s_waitcnt vmcnt(0)
	v_add_u32_e32 v146, 0x18000, v3
	v_add_u32_e32 v147, 0x18400, v3
	v_add_u32_e32 v148, 0x18800, v3
	v_add_u32_e32 v149, 0x18c00, v3
	v_add_u32_e32 v150, 0x1c000, v3
	v_add_u32_e32 v151, 0x1c400, v3
	v_add_u32_e32 v152, 0x1c800, v3
	v_add_u32_e32 v153, 0x1cc00, v3
	s_cselect_b64 s[6:7], -1, 0
	v_add_u32_e32 v154, s8, v2
	s_mov_b64 s[8:9], 0x48000
	s_mov_b64 s[10:11], 0x50000
	s_mov_b64 s[12:13], 0x58000
	s_mov_b64 s[18:19], s[22:23]
	s_mov_b64 s[20:21], s[24:25]
	s_barrier
	s_branch .LBB0_1708
	s_nop 0
	s_nop 0
	s_nop 0
	s_nop 0
	s_nop 0
	s_nop 0
	s_nop 0
	s_nop 0
	s_nop 0
	s_nop 0
	s_nop 0
	s_nop 0
	s_nop 0
	s_nop 0
	s_nop 0
